# adds: prologue weight transposes are taken off the workgroups that do both an adaLN unit and a hyena-filter item
# speedup vs baseline: 1.0055x; 1.0055x over previous
.LBB0_15:
	v_writelane_b32 v254, s83, 6
	v_writelane_b32 v254, s76, 7
	s_andn2_b64 vcc, exec, s[0:1]
	s_nop 0
	v_writelane_b32 v254, s77, 8
	s_cbranch_vccnz .LBB0_181
	s_mov_b32 s10, 0
	s_add_i32 s30, s10, s84
	v_add_u32_e32 v2, s10, v0
	s_ashr_i32 s11, s10, 31
	v_readfirstlane_b32 s0, v2
	s_ashr_i32 s1, s0, 6
	v_readlane_b32 s2, v254, 2
	v_readlane_b32 s3, v254, 3
	s_add_u32 s8, s2, s10
	s_addc_u32 s9, s3, s11
	s_lshl_b32 s2, s30, 3
	s_add_i32 s14, s2, s1
	s_lshl_b32 s33, s68, 3
	s_mov_b32 s101, s33
	s_cmp_lg_u32 s68, 0x100
	s_cbranch_scc1 .Lpre_std
	s_sub_i32 s2, s30, 80
	s_cmp_lt_u32 s30, 0x70
	s_cselect_b32 s2, s30, s2
	s_lshl_b32 s2, s2, 3
	s_add_i32 s14, s2, s1
	s_movk_i32 s101, 0x580
	s_sub_i32 s2, s30, 0x70
	s_cmp_lt_u32 s2, 80
	s_cselect_b32 s14, 0x7fff, s14
.Lpre_std:
	s_cmpk_gt_i32 s14, 0x201f
	v_and_b32_e32 v4, 63, v2
	s_cbranch_scc1 .LBB0_43
	s_lshl_b32 s1, s1, 14
	s_bfe_u32 s0, s0, 0x10006
	s_add_i32 s2, s1, 0
	s_lshl_b32 s15, s0, 20
	s_add_u32 s1, s8, s15
	s_addc_u32 s4, s9, 0
	s_add_u32 s18, s1, 0x2c00000
	s_addc_u32 s19, s4, 0
	s_mul_i32 s1, s0, 0x600000
	s_add_u32 s1, s8, s1
	s_addc_u32 s4, s9, 0
	s_add_u32 s21, s1, 0x2000000
	s_addc_u32 s22, s4, 0
	s_lshl_b32 s1, s0, 21
	s_add_u32 s1, s8, s1
	s_addc_u32 s4, s9, 0
	s_add_u32 s23, s1, 0x1c00000
	s_mul_i32 s20, s0, 0xc00000
	s_addc_u32 s24, s4, 0
	s_mul_i32 s25, s0, 0xc20000
	s_mul_i32 s0, s0, 0x700000
	s_add_u32 s0, s8, s0
	s_addc_u32 s1, s9, 0
	v_lshlrev_b32_e32 v3, 3, v4
	s_add_u32 s28, s0, 0xe00000
	v_lshrrev_b32_e32 v6, 5, v4
	v_and_b32_e32 v8, 31, v2
	v_lshrrev_b32_e32 v1, 3, v4
	v_and_b32_e32 v14, 56, v3
	s_addc_u32 s29, s1, 0
	s_lshl_b64 s[0:1], s[10:11], 3
	v_readlane_b32 s4, v254, 4
	v_lshl_add_u32 v12, v8, 2, s2
	v_mul_u32_u24_e32 v5, 0x84, v6
	v_mul_u32_u24_e32 v3, 0x84, v14
	v_lshlrev_b32_e32 v7, 2, v1
	v_readlane_b32 s5, v254, 5
	s_add_u32 s4, s4, s0
	v_mov_b32_e32 v9, 0
	v_add3_u32 v3, s2, v3, v7
	v_or_b32_e32 v7, 8, v1
	v_or_b32_e32 v13, 16, v1
	v_or_b32_e32 v30, 24, v1
	v_add_u32_e32 v5, v12, v5
	s_mov_b32 s3, 0
	s_addc_u32 s5, s5, s1
	v_lshlrev_b32_e32 v10, 12, v6
	v_mov_b32_e32 v11, v9
	s_movk_i32 s31, 0x84
	v_mov_b32_e32 v15, v9
	v_lshlrev_b32_e32 v16, 10, v1
	v_mov_b32_e32 v17, v9
	v_lshlrev_b32_e32 v18, 10, v7
	v_mov_b32_e32 v19, v9
	v_lshlrev_b32_e32 v20, 10, v13
	v_mov_b32_e32 v21, v9
	v_lshlrev_b32_e32 v22, 10, v30
	v_mov_b32_e32 v23, v9
	v_lshlrev_b32_e32 v24, 11, v1
	v_mov_b32_e32 v25, v9
	v_lshlrev_b32_e32 v26, 11, v7
	v_mov_b32_e32 v27, v9
	v_lshlrev_b32_e32 v28, 11, v13
	v_mov_b32_e32 v29, v9
	v_lshlrev_b32_e32 v30, 11, v30
	v_mov_b32_e32 v31, v9
	v_mov_b32_e32 v1, v6
	s_movk_i32 s34, 0x2000
	s_movk_i32 s35, 0x4000
	s_movk_i32 s36, 0x6000
	s_mov_b32 s37, 0x8000
	s_mov_b32 s38, 0xa000
	s_mov_b32 s39, 0xc000
	s_mov_b32 s40, 0xe000
	s_mov_b32 s41, 0x10000
	s_mov_b32 s42, 0x12000
	s_mov_b32 s43, 0x14000
	s_mov_b32 s44, 0x16000
	s_mov_b32 s45, 0x18000
	s_mov_b32 s46, 0x1a000
	s_mov_b32 s47, 0x1c000
	s_mov_b32 s48, 0x1e000
	s_mov_b32 s49, 0x20000
	s_mov_b32 s50, 0x22000
	s_mov_b32 s51, 0x24000
	s_mov_b32 s52, 0x26000
	s_mov_b32 s53, 0x28000
	s_mov_b32 s54, 0x2a000
	s_mov_b32 s55, 0x2c000
	s_mov_b32 s56, 0x2e000
	s_mov_b32 s57, 0x30000
	s_mov_b32 s58, 0x32000
	s_mov_b32 s59, 0x34000
	s_mov_b32 s60, 0x36000
	s_mov_b32 s61, 0x38000
	s_mov_b32 s62, 0x3a000
	s_mov_b32 s63, 0x3c000
	s_mov_b32 s64, 0x3e000
	s_mov_b32 s65, 0xc3e00000
	s_movk_i32 s66, 0x3000
	s_movk_i32 s67, 0x3080
	v_lshlrev_b32_e32 v32, 2, v8
	v_add_u32_e32 v7, 0x400, v5
	v_add_u32_e32 v13, 0x800, v5
	v_add_u32_e32 v36, 0xc00, v5
	v_add_u32_e32 v37, 0x1000, v5
	v_add_u32_e32 v38, 0x1400, v5
	v_add_u32_e32 v39, 0x1800, v5
	v_add_u32_e32 v40, 0x1c00, v5
	v_mov_b32_e32 v41, 0x43e00000
	s_branch .LBB0_19
.LBB0_18:
	s_add_i32 s14, s14, s101
	s_cmpk_gt_i32 s14, 0x201f
	s_cbranch_scc1 .LBB0_43
